# router bias load hoisted out of the norm2 pass loop; the per-pass full vmcnt wait became an LDS-only wait
# speedup vs baseline: 1.0010x; 1.0010x over previous
.LBB0_1134:
	s_andn2_b64 vcc, exec, s[4:5]
	s_cbranch_vccnz .LBB0_1345
	s_waitcnt vmcnt(16)
	v_mov_b32_e32 v136, v0
	s_nop 0
	v_readfirstlane_b32 s2, v136
	v_cmp_gt_i32_e64 s[40:41], 32, v136
	v_lshl_add_u32 v137, v136, 2, 0
	s_and_saveexec_b64 s[4:5], s[40:41]
	v_add_u32_e32 v2, 0x14c00, v137
	ds_write_b32 v2, v99
	s_or_b64 exec, exec, s[4:5]
	v_readlane_b32 s8, v255, 5
	s_ashr_i32 s6, s2, 6
	v_readlane_b32 s9, v255, 6
	v_readlane_b32 s2, v251, 8
	v_readlane_b32 s4, v255, 7
	s_mov_b32 s9, s69
	s_add_u32 s2, s2, s4
	v_readlane_b32 s4, v251, 9
	v_lshrrev_b32_e32 v2, 1, v136
	s_addc_u32 s10, s4, 0
	s_lshl_b64 s[4:5], s[8:9], 17
	v_readlane_b32 s7, v253, 24
	v_and_b32_e32 v2, 24, v2
	s_add_u32 s4, s7, s4
	v_readlane_b32 s7, v253, 25
	v_lshl_or_b32 v50, s6, 8, v2
	v_lshlrev_b32_e32 v2, 12, v136
	s_addc_u32 s5, s7, s5
	v_and_b32_e32 v98, 0xf000, v2
	v_lshl_add_u64 v[2:3], s[4:5], 0, v[98:99]
	s_mov_b64 s[4:5], 0x10000
	v_ashrrev_i32_e32 v51, 31, v50
	v_or_b32_e32 v12, 32, v50
	v_or_b32_e32 v18, 64, v50
	v_or_b32_e32 v28, 0x60, v50
	v_or_b32_e32 v34, 0x80, v50
	v_or_b32_e32 v44, 0xa0, v50
	v_or_b32_e32 v52, 0xc0, v50
	v_or_b32_e32 v62, 0xe0, v50
	v_lshl_add_u64 v[58:59], v[2:3], 0, s[4:5]
	v_lshlrev_b64 v[4:5], 1, v[50:51]
	v_ashrrev_i32_e32 v13, 31, v12
	v_ashrrev_i32_e32 v19, 31, v18
	v_ashrrev_i32_e32 v29, 31, v28
	v_ashrrev_i32_e32 v35, 31, v34
	v_ashrrev_i32_e32 v45, 31, v44
	v_ashrrev_i32_e32 v53, 31, v52
	v_ashrrev_i32_e32 v63, 31, v62
	v_lshl_add_u64 v[54:55], v[2:3], 0, v[4:5]
	s_waitcnt lgkmcnt(0)
	v_lshl_add_u64 v[10:11], v[58:59], 0, v[4:5]
	v_lshl_add_u64 v[14:15], v[12:13], 1, v[58:59]
	v_lshl_add_u64 v[26:27], v[18:19], 1, v[58:59]
	v_lshl_add_u64 v[30:31], v[28:29], 1, v[58:59]
	v_lshl_add_u64 v[42:43], v[34:35], 1, v[58:59]
	v_lshl_add_u64 v[46:47], v[44:45], 1, v[58:59]
	v_lshl_add_u64 v[60:61], v[52:53], 1, v[58:59]
	v_lshl_add_u64 v[62:63], v[62:63], 1, v[58:59]
	global_load_dwordx4 v[2:5], v[54:55], off
	global_load_dwordx4 v[6:9], v[54:55], off offset:64
	s_nop 0
	global_load_dwordx4 v[10:13], v[10:11], off
	s_nop 0
	global_load_dwordx4 v[14:17], v[14:15], off
	s_nop 0
	global_load_dwordx4 v[18:21], v[54:55], off offset:128
	global_load_dwordx4 v[22:25], v[54:55], off offset:192
	s_nop 0
	global_load_dwordx4 v[26:29], v[26:27], off
	s_nop 0
	global_load_dwordx4 v[30:33], v[30:31], off
	s_nop 0
	global_load_dwordx4 v[34:37], v[54:55], off offset:256
	global_load_dwordx4 v[38:41], v[54:55], off offset:320
	s_nop 0
	global_load_dwordx4 v[42:45], v[42:43], off
	s_nop 0
	global_load_dwordx4 v[46:49], v[46:47], off
	s_nop 0
	global_load_dwordx4 v[50:53], v[54:55], off offset:384
	s_nop 0
	global_load_dwordx4 v[54:57], v[54:55], off offset:448
	s_nop 0
	global_load_dwordx4 v[58:61], v[60:61], off
	s_nop 0
	global_load_dwordx4 v[62:65], v[62:63], off
	v_and_b32_e32 v181, 31, v136
	v_cmp_ne_u32_e32 vcc, 0, v181
	v_readlane_b32 s4, v251, 10
	v_readlane_b32 s12, v254, 53
	v_cndmask_b32_e64 v185, 0, 1, vcc
	v_cmp_lt_u32_e32 vcc, 1, v181
	v_readlane_b32 s5, v251, 11
	v_readlane_b32 s13, v254, 54
	v_cndmask_b32_e64 v186, 0, 1, vcc
	v_cmp_lt_u32_e32 vcc, 2, v181
	s_and_b64 s[4:5], s[4:5], s[12:13]
	s_and_b64 s[4:5], s[4:5], exec
	v_cndmask_b32_e64 v187, 0, 1, vcc
	v_cmp_lt_u32_e32 vcc, 3, v181
	v_and_b32_e32 v138, 63, v136
	v_readlane_b32 s4, v251, 4
	v_cndmask_b32_e64 v188, 0, 1, vcc
	v_cmp_lt_u32_e32 vcc, 4, v181
	v_lshlrev_b32_e32 v98, 3, v138
	v_readlane_b32 s5, v251, 5
	v_cndmask_b32_e64 v189, 0, 1, vcc
	v_cmp_lt_u32_e32 vcc, 5, v181
	v_lshlrev_b32_e32 v66, 2, v138
	v_mov_b32_e32 v67, v99
	v_cndmask_b32_e64 v190, 0, 1, vcc
	v_cmp_lt_u32_e32 vcc, 6, v181
	s_waitcnt vmcnt(16)
	v_lshl_add_u64 v[140:141], s[4:5], 0, v[98:99]
	v_lshl_add_u64 v[142:143], s[76:77], 0, v[66:67]
	v_cndmask_b32_e64 v191, 0, 1, vcc
	v_cmp_lt_u32_e32 vcc, 7, v181
	v_lshlrev_b32_e32 v66, 2, v136
	v_readlane_b32 s4, v254, 26
	v_cndmask_b32_e64 v192, 0, 1, vcc
	v_cmp_lt_u32_e32 vcc, 8, v181
	s_cselect_b32 s11, 5, 4
	s_lshl_b32 s12, s6, 1
	v_cndmask_b32_e64 v193, 0, 1, vcc
	v_cmp_lt_u32_e32 vcc, 9, v181
	v_add_u32_e32 v180, s4, v66
	s_lshl_b32 s4, s6, 9
	v_cndmask_b32_e64 v194, 0, 1, vcc
	v_cmp_lt_u32_e32 vcc, 10, v181
	s_lshl_b32 s5, s6, 11
	v_readlane_b32 s6, v254, 20
	v_cndmask_b32_e64 v195, 0, 1, vcc
	v_cmp_lt_u32_e32 vcc, 11, v181
	v_and_b32_e32 v67, 15, v136
	s_add_i32 s5, s5, s6
	v_cndmask_b32_e64 v201, 0, 1, vcc
	v_cmp_lt_u32_e32 vcc, 12, v181
	v_mul_u32_u24_e32 v68, 0x1010, v67
	v_lshl_add_u32 v67, v67, 2, s5
	v_cndmask_b32_e64 v202, 0, 1, vcc
	v_cmp_lt_u32_e32 vcc, 13, v181
	v_and_b32_e32 v70, 0xffffff80, v66
	v_lshlrev_b32_e32 v71, 2, v181
	v_cndmask_b32_e64 v203, 0, 1, vcc
	v_cmp_lt_u32_e32 vcc, 14, v181
	v_readlane_b32 s5, v254, 27
	v_and_b32_e32 v69, 48, v136
	v_cndmask_b32_e64 v204, 0, 1, vcc
	v_cmp_lt_u32_e32 vcc, 15, v181
	v_add3_u32 v182, s6, v70, v71
	v_add_u32_e32 v183, s5, v66
	v_cndmask_b32_e64 v205, 0, 1, vcc
	v_cmp_lt_u32_e32 vcc, 16, v181
	v_add_u32_e32 v184, s5, v70
	s_add_i32 s5, 0, 0x14c00
	v_cndmask_b32_e64 v206, 0, 1, vcc
	v_cmp_lt_u32_e32 vcc, 17, v181
	v_ashrrev_i32_e32 v70, 3, v136
	v_add3_u32 v68, 0, v68, v69
	v_cndmask_b32_e64 v207, 0, 1, vcc
	v_cmp_lt_u32_e32 vcc, 18, v181
	v_lshlrev_b32_e32 v69, 5, v136
	s_mov_b32 s18, s8
	v_cndmask_b32_e64 v208, 0, 1, vcc
	v_cmp_lt_u32_e32 vcc, 19, v181
	v_add_u32_e32 v238, s5, v71
	v_and_b32_e32 v239, -4, v70
	v_cndmask_b32_e64 v209, 0, 1, vcc
	v_cmp_lt_u32_e32 vcc, 20, v181
	v_and_b32_e32 v70, 0x3ffffffc, v136
	v_readlane_b32 s5, v254, 28
	v_cndmask_b32_e64 v210, 0, 1, vcc
	v_cmp_lt_u32_e32 vcc, 21, v181
	v_and_b32_e32 v69, 0x600, v69
	v_writelane_b32 v255, s18, 5
	v_cndmask_b32_e64 v211, 0, 1, vcc
	v_cmp_lt_u32_e32 vcc, 22, v181
	v_and_b32_e32 v240, 3, v136
	v_lshl_add_u32 v241, v70, 2, s5
	v_cndmask_b32_e64 v212, 0, 1, vcc
	v_cmp_lt_u32_e32 vcc, 23, v181
	v_readlane_b32 s5, v254, 29
	s_lshl_b32 s68, s8, 11
	v_cndmask_b32_e64 v213, 0, 1, vcc
	v_cmp_lt_u32_e32 vcc, 24, v181
	v_add_u32_e32 v139, 0, v98
	v_writelane_b32 v255, s19, 6
	v_cndmask_b32_e64 v214, 0, 1, vcc
	v_cmp_lt_u32_e32 vcc, 25, v181
	v_lshl_or_b32 v144, s8, 5, v181
	v_mov_b32_e32 v145, v99
	v_cndmask_b32_e64 v215, 0, 1, vcc
	v_cmp_lt_u32_e32 vcc, 26, v181
	s_mov_b32 s13, 0
	v_cmp_gt_i32_e64 s[42:43], 64, v136
	v_cndmask_b32_e64 v216, 0, 1, vcc
	v_cmp_lt_u32_e32 vcc, 27, v181
	v_cmp_eq_u32_e64 s[44:45], 2, v240
	v_add_u32_e32 v242, s5, v66
	v_cndmask_b32_e64 v217, 0, 1, vcc
	v_cmp_lt_u32_e32 vcc, 28, v181
	v_lshlrev_b32_e32 v98, 4, v138
	v_add_u32_e32 v243, s4, v68
	v_cndmask_b32_e64 v218, 0, 1, vcc
	v_cmp_lt_u32_e32 vcc, 29, v181
	v_add_u32_e32 v244, v67, v69
	s_nop 0
	v_cndmask_b32_e64 v219, 0, 1, vcc
	v_cmp_eq_u32_e32 vcc, 31, v181
	s_nop 1
	v_cndmask_b32_e64 v237, 0, 1, vcc
	s_load_dwordx2 s[4:5], s[0:1], 0xb8
	s_waitcnt lgkmcnt(0)
	v_lshl_add_u64 v[248:249], v[144:145], 2, s[4:5]
	global_load_dword v246, v[248:249], off
	s_branch .LBB0_1141

.LBB0_1144:
	s_or_b32 s7, s6, s12
	s_add_i32 s8, s7, s17
	s_ashr_i32 s9, s8, 31
	v_cndmask_b32_e64 v134, 0, 1, s[4:5]
	s_lshl_b64 s[4:5], s[8:9], 11
	s_lshl_b64 s[8:9], s[8:9], 12
	v_lshl_add_u64 v[132:133], v[140:141], 0, s[8:9]
	global_load_dwordx2 v[148:149], v[132:133], off
	global_load_dwordx2 v[150:151], v[132:133], off offset:512
	global_load_dwordx2 v[152:153], v[132:133], off offset:1024
	global_load_dwordx2 v[146:147], v[132:133], off offset:1536
	global_load_dwordx2 v[154:155], v[132:133], off offset:2048
	global_load_dwordx2 v[178:179], v[132:133], off offset:2560
	global_load_dwordx2 v[196:197], v[132:133], off offset:3072
	s_nop 0
	global_load_dwordx2 v[132:133], v[132:133], off offset:3584
	v_cmp_ne_u32_e64 s[46:47], 1, v134
	s_mulk_i32 s7, 0x1010
	s_waitcnt vmcnt(7)
	v_and_b32_e32 v177, 0xffff0000, v149
	v_and_b32_e32 v175, 0xffff0000, v148
	v_lshlrev_b32_e32 v176, 16, v149
	s_waitcnt vmcnt(4)
	v_lshlrev_b32_e32 v165, 16, v146
	v_and_b32_e32 v163, 0xffff0000, v146
	v_lshlrev_b32_e32 v160, 16, v147
	v_and_b32_e32 v161, 0xffff0000, v147
	s_waitcnt vmcnt(0)
	v_lshlrev_b32_e32 v147, 16, v132
	v_mul_f32_e32 v146, v177, v177
	v_lshlrev_b32_e32 v174, 16, v148
	v_pk_fma_f32 v[148:149], v[176:177], v[176:177], v[146:147] op_sel_hi:[1,1,0]
	v_and_b32_e32 v173, 0xffff0000, v151
	v_and_b32_e32 v172, 0xffff0000, v150
	v_mul_f32_e32 v146, v175, v175
	v_lshlrev_b32_e32 v171, 16, v151
	v_lshlrev_b32_e32 v170, 16, v150
	v_pk_mul_f32 v[150:151], v[172:173], v[172:173]
	v_lshlrev_b32_e32 v166, 16, v152
	v_and_b32_e32 v167, 0xffff0000, v152
	v_lshlrev_b32_e32 v168, 16, v153
	v_and_b32_e32 v169, 0xffff0000, v153
	v_pk_fma_f32 v[152:153], v[174:175], v[174:175], v[146:147] op_sel_hi:[1,1,0]
	v_pk_fma_f32 v[150:151], v[170:171], v[170:171], v[150:151]
	v_mov_b32_e32 v164, v152
	v_mov_b32_e32 v156, v148
	v_mov_b32_e32 v157, v165
	v_mul_f32_e32 v158, v163, v163
	v_pk_add_f32 v[148:149], v[152:153], v[148:149]
	v_pk_mul_f32 v[152:153], v[164:165], v[156:157]
	v_pk_add_f32 v[150:151], v[150:151], v[150:151] op_sel:[0,1] op_sel_hi:[1,0]
	v_mov_b32_e32 v149, v153
	v_mov_b32_e32 v151, v158
	v_mul_f32_e32 v146, v167, v167
	v_pk_add_f32 v[148:149], v[148:149], v[150:151]
	v_pk_fma_f32 v[150:151], v[166:167], v[166:167], v[146:147] op_sel_hi:[1,1,0]
	v_mul_f32_e32 v146, v169, v169
	v_mul_f32_e32 v159, v160, v160
	v_mul_f32_e32 v162, v161, v161
	v_pk_fma_f32 v[152:153], v[168:169], v[168:169], v[146:147] op_sel_hi:[1,1,0]
	v_mov_b32_e32 v151, v159
	v_mov_b32_e32 v153, v162
	v_pk_add_f32 v[150:151], v[150:151], v[152:153]
	v_and_b32_e32 v159, 0xffff0000, v155
	v_and_b32_e32 v158, 0xffff0000, v154
	v_pk_add_f32 v[226:227], v[148:149], v[150:151]
	v_lshlrev_b32_e32 v157, 16, v155
	v_lshlrev_b32_e32 v156, 16, v154
	v_pk_mul_f32 v[148:149], v[158:159], v[158:159]
	v_and_b32_e32 v155, 0xffff0000, v179
	v_pk_fma_f32 v[148:149], v[156:157], v[156:157], v[148:149]
	v_and_b32_e32 v154, 0xffff0000, v178
	v_pk_add_f32 v[228:229], v[148:149], v[148:149] op_sel:[0,1] op_sel_hi:[1,0]
	v_lshlrev_b32_e32 v153, 16, v179
	v_lshlrev_b32_e32 v152, 16, v178
	v_pk_mul_f32 v[148:149], v[154:155], v[154:155]
	v_lshlrev_b32_e32 v150, 16, v197
	v_pk_fma_f32 v[178:179], v[152:153], v[152:153], v[148:149]
	v_lshlrev_b32_e32 v148, 16, v196
	v_and_b32_e32 v149, 0xffff0000, v196
	v_and_b32_e32 v151, 0xffff0000, v197
	v_pk_add_f32 v[196:197], v[226:227], v[226:227] op_sel:[0,1] op_sel_hi:[1,0]
	v_and_b32_e32 v135, 0xffff0000, v132
	v_mov_b32_e32 v146, v196
	v_mov_b32_e32 v226, v228
	v_mov_b32_e32 v227, v147
	v_mul_f32_e32 v162, v135, v135
	v_pk_add_f32 v[196:197], v[196:197], v[228:229]
	v_pk_mul_f32 v[226:227], v[146:147], v[226:227]
	v_pk_add_f32 v[178:179], v[178:179], v[178:179] op_sel:[0,1] op_sel_hi:[1,0]
	v_mov_b32_e32 v197, v227
	v_mov_b32_e32 v179, v162
	v_mul_f32_e32 v146, v149, v149
	v_lshlrev_b32_e32 v132, 16, v133
	v_and_b32_e32 v133, 0xffff0000, v133
	v_pk_add_f32 v[178:179], v[196:197], v[178:179]
	v_pk_fma_f32 v[196:197], v[148:149], v[148:149], v[146:147] op_sel_hi:[1,1,0]
	v_mul_f32_e32 v146, v151, v151
	v_mul_f32_e32 v164, v132, v132
	v_mul_f32_e32 v245, v133, v133
	v_pk_fma_f32 v[226:227], v[150:151], v[150:151], v[146:147] op_sel_hi:[1,1,0]
	v_mov_b32_e32 v197, v164
	v_mov_b32_e32 v227, v245
	v_pk_add_f32 v[196:197], v[196:197], v[226:227]
	s_nop 0
	v_pk_add_f32 v[178:179], v[178:179], v[196:197]
	s_nop 0
	v_add_f32_e32 v146, v178, v179
	s_nop 1
	v_add_f32_dpp v146, v146, v146 quad_perm:[1,0,3,2] row_mask:0xf bank_mask:0xf bound_ctrl:1
	s_nop 1
	v_add_f32_dpp v146, v146, v146 quad_perm:[2,3,0,1] row_mask:0xf bank_mask:0xf bound_ctrl:1
	s_nop 1
	v_add_f32_dpp v146, v146, v146 row_half_mirror row_mask:0xf bank_mask:0xf bound_ctrl:1
	s_nop 1
	v_add_f32_dpp v146, v146, v146 row_mirror row_mask:0xf bank_mask:0xf bound_ctrl:1
	s_nop 0
	v_readlane_b32 s6, v146, 16
	v_readlane_b32 s18, v146, 48
	v_readlane_b32 s8, v146, 0
	v_readlane_b32 s9, v146, 32
	v_mov_b32_e32 v178, s6
	v_mov_b32_e32 v179, s18
	v_pk_add_f32 v[178:179], s[8:9], v[178:179]
	s_mov_b32 s6, 1
	v_add_f32_e32 v146, v178, v179
	v_fmamk_f32 v146, v146, 0x3a000000, v1
	v_cmp_gt_f32_e32 vcc, s33, v146
	v_mul_f32_e32 v162, 0x4f800000, v146
	s_nop 0
	v_cndmask_b32_e32 v146, v146, v162, vcc
	v_sqrt_f32_e32 v162, v146
	s_nop 0
	v_add_u32_e32 v178, -1, v162
	v_fma_f32 v134, -v178, v162, v146
	v_add_u32_e32 v164, 1, v162
	v_cmp_ge_f32_e64 s[48:49], 0, v134
	s_nop 1
	v_cndmask_b32_e64 v134, v162, v178, s[48:49]
	v_fma_f32 v162, -v164, v162, v146
	v_cmp_lt_f32_e64 s[48:49], 0, v162
	s_nop 1
	v_cndmask_b32_e64 v134, v134, v164, s[48:49]
	v_mul_f32_e32 v162, 0x37800000, v134
	v_cndmask_b32_e32 v134, v134, v162, vcc
	v_cmp_class_f32_e32 vcc, v146, v220
	s_nop 1
	v_cndmask_b32_e32 v134, v134, v146, vcc
	v_div_scale_f32 v146, s[8:9], v134, v134, 1.0
	v_rcp_f32_e32 v162, v146
	s_nop 0
	v_fma_f32 v164, -v146, v162, 1.0
	v_fmac_f32_e32 v162, v164, v162
	v_div_scale_f32 v164, vcc, 1.0, v134, 1.0
	v_mul_f32_e32 v178, v164, v162
	v_fma_f32 v179, -v146, v178, v164
	v_fmac_f32_e32 v178, v179, v162
	v_fma_f32 v146, -v146, v178, v164
	v_div_fmas_f32 v146, v146, v162, v178
	v_div_fixup_f32 v146, v146, v134, 1.0
	v_pk_mul_f32 v[174:175], v[146:147], v[174:175] op_sel_hi:[0,1]
	v_pk_fma_f32 v[174:175], v[70:71], v[174:175], v[66:67]
	v_mov_b32_e32 v134, v99
	v_cvt_pk_fp8_f32 v134, v174, v175
	v_pk_mul_f32 v[176:177], v[146:147], v[176:177] op_sel_hi:[0,1]
	v_pk_fma_f32 v[176:177], v[72:73], v[176:177], v[68:69]
	v_cvt_pk_bf16_f32 v196, v174, v175
	v_cvt_pk_fp8_f32 v134, v176, v177 op_sel:[0,0,1]
	v_mov_b32_e32 v174, v170
	v_mov_b32_e32 v175, v172
	v_lshl_add_u64 v[178:179], v[142:143], 0, s[4:5]
	v_pk_mul_f32 v[174:175], v[146:147], v[174:175] op_sel_hi:[0,1]
	v_mov_b32_e32 v172, v171
	global_store_dword v[178:179], v134, off
	v_pk_mul_f32 v[170:171], v[146:147], v[172:173] op_sel_hi:[0,1]
	v_pk_fma_f32 v[172:173], v[78:79], v[174:175], v[74:75]
	v_mov_b32_e32 v134, v99
	v_cvt_pk_fp8_f32 v134, v172, v173
	v_pk_fma_f32 v[170:171], v[80:81], v[170:171], v[76:77]
	v_pk_mul_f32 v[166:167], v[146:147], v[166:167] op_sel_hi:[0,1]
	v_pk_fma_f32 v[166:167], v[86:87], v[166:167], v[82:83]
	v_cvt_pk_fp8_f32 v134, v170, v171 op_sel:[0,0,1]
	v_pk_mul_f32 v[168:169], v[146:147], v[168:169] op_sel_hi:[0,1]
	v_pk_fma_f32 v[168:169], v[88:89], v[168:169], v[84:85]
	v_mov_b32_e32 v162, v165
	global_store_dword v[178:179], v134, off offset:256
	v_mov_b32_e32 v134, v99
	v_cvt_pk_fp8_f32 v134, v166, v167
	v_pk_mul_f32 v[162:163], v[162:163], v[146:147] op_sel_hi:[1,0]
	v_pk_mul_f32 v[160:161], v[160:161], v[146:147] op_sel_hi:[1,0]
	v_pk_fma_f32 v[162:163], v[94:95], v[162:163], v[90:91]
	v_cvt_pk_fp8_f32 v134, v168, v169 op_sel:[0,0,1]
	v_pk_fma_f32 v[160:161], v[96:97], v[160:161], v[92:93]
	v_cvt_pk_bf16_f32 v175, v170, v171
	v_cvt_pk_bf16_f32 v170, v166, v167
	global_store_dword v[178:179], v134, off offset:512
	v_mov_b32_e32 v134, v99
	v_cvt_pk_fp8_f32 v134, v162, v163
	v_cvt_pk_bf16_f32 v167, v160, v161
	v_pk_mul_f32 v[148:149], v[146:147], v[148:149] op_sel_hi:[0,1]
	v_pk_fma_f32 v[148:149], v[120:121], v[148:149], v[116:117]
	v_cvt_pk_fp8_f32 v134, v160, v161 op_sel:[0,0,1]
	v_mov_b32_e32 v160, v156
	v_mov_b32_e32 v161, v158
	v_pk_mul_f32 v[160:161], v[146:147], v[160:161] op_sel_hi:[0,1]
	v_mov_b32_e32 v158, v157
	global_store_dword v[178:179], v134, off offset:768
	v_pk_mul_f32 v[156:157], v[146:147], v[158:159] op_sel_hi:[0,1]
	v_pk_fma_f32 v[158:159], v[104:105], v[160:161], v[100:101]
	v_mov_b32_e32 v134, v99
	v_cvt_pk_fp8_f32 v134, v158, v159
	v_pk_fma_f32 v[156:157], v[106:107], v[156:157], v[102:103]
	v_pk_mul_f32 v[150:151], v[146:147], v[150:151] op_sel_hi:[0,1]
	v_cvt_pk_bf16_f32 v161, v156, v157
	v_cvt_pk_fp8_f32 v134, v156, v157 op_sel:[0,0,1]
	v_mov_b32_e32 v156, v152
	v_mov_b32_e32 v157, v154
	v_pk_mul_f32 v[156:157], v[146:147], v[156:157] op_sel_hi:[0,1]
	v_mov_b32_e32 v154, v153
	global_store_dword v[178:179], v134, off offset:1024
	v_pk_mul_f32 v[152:153], v[146:147], v[154:155] op_sel_hi:[0,1]
	v_pk_fma_f32 v[154:155], v[112:113], v[156:157], v[108:109]
	v_mov_b32_e32 v134, v99
	v_cvt_pk_fp8_f32 v134, v154, v155
	v_pk_fma_f32 v[152:153], v[114:115], v[152:153], v[110:111]
	v_pk_fma_f32 v[150:151], v[122:123], v[150:151], v[118:119]
	v_pk_mul_f32 v[132:133], v[132:133], v[146:147] op_sel_hi:[1,0]
	v_cvt_pk_fp8_f32 v134, v152, v153 op_sel:[0,0,1]
	v_pk_fma_f32 v[132:133], v[130:131], v[132:133], v[126:127]
	v_add_u32_e32 v164, s7, v139
	v_cvt_pk_bf16_f32 v157, v152, v153
	global_store_dword v[178:179], v134, off offset:1280
	v_mov_b32_e32 v134, v99
	v_cvt_pk_fp8_f32 v134, v148, v149
	v_cvt_pk_bf16_f32 v152, v148, v149
	v_cvt_pk_bf16_f32 v153, v150, v151
	v_cvt_pk_bf16_f32 v197, v176, v177
	v_cvt_pk_fp8_f32 v134, v150, v151 op_sel:[0,0,1]
	v_cvt_pk_bf16_f32 v174, v172, v173
	v_cvt_pk_bf16_f32 v171, v168, v169
	v_cvt_pk_bf16_f32 v166, v162, v163
	global_store_dword v[178:179], v134, off offset:1536
	v_mov_b32_e32 v134, v147
	v_pk_mul_f32 v[134:135], v[134:135], v[146:147] op_sel_hi:[1,0]
	v_cvt_pk_bf16_f32 v147, v132, v133
	v_pk_fma_f32 v[134:135], v[128:129], v[134:135], v[124:125]
	v_cvt_pk_bf16_f32 v160, v158, v159
	v_cvt_pk_bf16_f32 v146, v134, v135
	ds_write2st64_b64 v164, v[152:153], v[146:147] offset0:6 offset1:7
	v_mov_b32_e32 v146, v99
	v_cvt_pk_fp8_f32 v146, v134, v135
	v_cvt_pk_bf16_f32 v156, v154, v155
	s_mov_b64 s[4:5], 0
	s_and_b64 vcc, exec, s[46:47]
	v_cvt_pk_fp8_f32 v146, v132, v133 op_sel:[0,0,1]
	ds_write2st64_b64 v164, v[196:197], v[174:175] offset1:1
	ds_write2st64_b64 v164, v[170:171], v[166:167] offset0:2 offset1:3
	ds_write2st64_b64 v164, v[160:161], v[156:157] offset0:4 offset1:5
	global_store_dword v[178:179], v146, off offset:1792
	s_cbranch_vccz .LBB0_1144
	s_waitcnt lgkmcnt(0)
	s_barrier
	ds_read_b128 v[132:135], v243
	ds_read_b128 v[150:153], v243 offset:64
	s_waitcnt lgkmcnt(1)
	v_mfma_f32_16x16x32_bf16 v[146:149], v[132:135], v[2:5], 0
	v_mfma_f32_16x16x32_bf16 v[132:135], v[132:135], v[10:13], 0
	s_waitcnt lgkmcnt(0)
	v_mfma_f32_16x16x32_bf16 v[146:149], v[150:153], v[6:9], v[146:149]
	v_mfma_f32_16x16x32_bf16 v[132:135], v[150:153], v[14:17], v[132:135]
	ds_read_b128 v[150:153], v243 offset:128
	s_waitcnt lgkmcnt(0)
	v_mfma_f32_16x16x32_bf16 v[146:149], v[150:153], v[18:21], v[146:149]
	v_mfma_f32_16x16x32_bf16 v[132:135], v[150:153], v[26:29], v[132:135]
	ds_read_b128 v[150:153], v243 offset:192
	s_waitcnt lgkmcnt(0)
	v_mfma_f32_16x16x32_bf16 v[146:149], v[150:153], v[22:25], v[146:149]
	v_mfma_f32_16x16x32_bf16 v[132:135], v[150:153], v[30:33], v[132:135]
	ds_read_b128 v[150:153], v243 offset:256
	s_waitcnt lgkmcnt(0)
	v_mfma_f32_16x16x32_bf16 v[146:149], v[150:153], v[34:37], v[146:149]
	v_mfma_f32_16x16x32_bf16 v[132:135], v[150:153], v[42:45], v[132:135]
	ds_read_b128 v[150:153], v243 offset:320
	s_waitcnt lgkmcnt(0)
	v_mfma_f32_16x16x32_bf16 v[146:149], v[150:153], v[38:41], v[146:149]
	v_mfma_f32_16x16x32_bf16 v[132:135], v[150:153], v[46:49], v[132:135]
	ds_read_b128 v[150:153], v243 offset:384
	s_waitcnt lgkmcnt(0)
	v_mfma_f32_16x16x32_bf16 v[146:149], v[150:153], v[50:53], v[146:149]
	v_mfma_f32_16x16x32_bf16 v[132:135], v[150:153], v[58:61], v[132:135]
	ds_read_b128 v[150:153], v243 offset:448
	s_waitcnt lgkmcnt(0)
	v_mfma_f32_16x16x32_bf16 v[146:149], v[150:153], v[54:57], v[146:149]
	v_mfma_f32_16x16x32_bf16 v[132:135], v[150:153], v[62:65], v[132:135]
	s_nop 7
	ds_write2_b32 v244, v146, v132 offset1:16
	ds_write2_b32 v244, v147, v133 offset0:32 offset1:48
	ds_write2_b32 v244, v148, v134 offset0:64 offset1:80
	ds_write2_b32 v244, v149, v135 offset0:96 offset1:112
	s_waitcnt lgkmcnt(0)
	s_barrier
	v_mov_b32_e32 v147, 1
	v_mov_b32_e32 v148, 1
	s_waitcnt lgkmcnt(0)
	v_mov_b32_e32 v134, v246
	ds_read2st64_b32 v[132:133], v182 offset1:8
	s_waitcnt lgkmcnt(0)
	v_add_f32_e32 v132, v134, v132
	v_add_f32_e32 v134, v132, v133
	ds_read2st64_b32 v[132:133], v182 offset0:16 offset1:24
	s_waitcnt lgkmcnt(0)
	v_add_f32_e32 v132, v134, v132
	v_add_f32_e32 v134, v132, v133
	ds_read2st64_b32 v[132:133], v182 offset0:32 offset1:40
	s_waitcnt lgkmcnt(0)
	v_add_f32_e32 v132, v134, v132
	v_add_f32_e32 v134, v132, v133
	ds_read2st64_b32 v[132:133], v182 offset0:48 offset1:56
	s_waitcnt lgkmcnt(0)
	v_add_f32_e32 v132, v134, v132
	v_add_f32_e32 v132, v132, v133
	ds_write_b32 v183, v132
	s_waitcnt lgkmcnt(0)
	s_barrier
	ds_read_b32 v146, v183
	ds_read_b128 v[132:135], v184
	s_waitcnt lgkmcnt(0)
	v_cmp_ngt_f32_e32 vcc, v132, v146
	s_and_saveexec_b64 s[4:5], vcc
	s_cbranch_execz .LBB0_1149
	v_cmp_eq_f32_e32 vcc, v132, v146
	v_mov_b32_e32 v148, 0
	s_and_saveexec_b64 s[6:7], vcc
	v_mov_b32_e32 v148, v185
	s_or_b64 exec, exec, s[6:7]
